# pre-norm phase: per-row 64-lane sum via DPP row rotations + readlanes instead of six ds_bpermute hops (on top of the DPP scan)
# baseline (speedup 1.0000x reference)
.LBB0_168:
	v_lshlrev_b32_e32 v91, 16, v57
	v_lshlrev_b32_e32 v90, 16, v56
	v_and_b32_e32 v57, 0xffff0000, v57
	v_and_b32_e32 v56, 0xffff0000, v56
	v_pk_mul_f32 v[98:99], v[56:57], v[56:57]
	v_lshlrev_b32_e32 v93, 16, v55
	v_lshlrev_b32_e32 v92, 16, v54
	v_and_b32_e32 v55, 0xffff0000, v55
	v_and_b32_e32 v54, 0xffff0000, v54
	v_pk_fma_f32 v[98:99], v[90:91], v[90:91], v[98:99]
	v_lshlrev_b32_e32 v94, 16, v52
	v_and_b32_e32 v95, 0xffff0000, v52
	v_lshlrev_b32_e32 v52, 16, v53
	v_lshlrev_b32_e32 v96, 16, v50
	v_pk_add_f32 v[98:99], v[98:99], v[98:99] op_sel_hi:[0,1]
	v_pk_mul_f32 v[100:101], v[54:55], v[54:55]
	v_and_b32_e32 v53, 0xffff0000, v53
	v_pk_fma_f32 v[100:101], v[92:93], v[92:93], v[100:101]
	v_mul_f32_e32 v97, v94, v94
	v_mul_f32_e32 v103, v95, v95
	v_mul_f32_e32 v98, v52, v52
	v_mov_b32_e32 v102, v96
	v_and_b32_e32 v108, 0xffff0000, v50
	v_lshlrev_b32_e32 v50, 16, v51
	v_and_b32_e32 v51, 0xffff0000, v51
	v_pk_add_f32 v[100:101], v[100:101], v[100:101] op_sel_hi:[0,1]
	v_pk_fma_f32 v[104:105], v[52:53], v[52:53], v[98:99] op_sel_hi:[1,1,0]
	v_pk_add_f32 v[102:103], v[96:97], v[102:103]
	v_mul_f32_e32 v104, v108, v108
	v_mul_f32_e32 v100, v50, v50
	v_mul_f32_e32 v98, v51, v51
	v_mul_f32_e32 v106, v96, v96
	v_mov_b32_e32 v107, v103
	v_pk_add_f32 v[102:103], v[106:107], v[104:105]
	v_pk_add_f32 v[98:99], v[100:101], v[98:99]
	s_add_i32 s0, s4, 3
	v_pk_add_f32 v[98:99], v[102:103], v[98:99]
	v_mov_b32_e32 v102, v90
	v_add_f32_e32 v97, v98, v99
	s_nop 1
	v_add_f32_dpp v97, v97, v97 row_ror:8 row_mask:0xf bank_mask:0xf
	s_nop 1
	v_add_f32_dpp v97, v97, v97 row_ror:4 row_mask:0xf bank_mask:0xf
	s_nop 1
	v_add_f32_dpp v97, v97, v97 row_ror:2 row_mask:0xf bank_mask:0xf
	s_nop 1
	v_add_f32_dpp v97, v97, v97 row_ror:1 row_mask:0xf bank_mask:0xf
	s_nop 0
	v_readlane_b32 s14, v97, 0
	v_readlane_b32 s15, v97, 16
	v_readlane_b32 s16, v97, 32
	v_readlane_b32 s17, v97, 48
	v_mov_b32_e32 v97, s14
	v_add_f32_e32 v97, s15, v97
	v_add_f32_e32 v97, s16, v97
	v_add_f32_e32 v97, s17, v97
	v_mov_b32_e32 v103, v56
	v_mov_b32_e32 v90, 0
	v_mov_b32_e32 v56, v91
	v_mov_b32_e32 v91, 0
	s_ashr_i32 s1, s0, 31
	s_lshl_b64 s[0:1], s[0:1], 10
	v_lshl_add_u64 v[100:101], v[24:25], 0, s[0:1]
	s_add_i32 s13, s13, 4
	s_and_b64 vcc, exec, s[2:3]
	v_fmamk_f32 v97, v97, 0x3a800000, v210
	v_rsq_f32_e32 v98, v97
	v_mov_b32_e32 v97, v108
	v_pk_mul_f32 v[102:103], v[98:99], v[102:103] op_sel_hi:[0,1]
	v_pk_fma_f32 v[102:103], v[28:29], v[102:103], v[4:5]
	v_pk_mul_f32 v[56:57], v[98:99], v[56:57] op_sel_hi:[0,1]
	v_cvt_pk_fp8_f32 v90, v102, v103
	v_pk_fma_f32 v[56:57], v[26:27], v[56:57], v[6:7]
	v_pk_mul_f32 v[52:53], v[52:53], v[98:99] op_sel_hi:[1,0]
	v_pk_mul_f32 v[50:51], v[50:51], v[98:99] op_sel_hi:[1,0]
	v_cvt_pk_fp8_f32 v90, v56, v57 op_sel:[0,0,1]
	v_mov_b32_e32 v56, v92
	v_mov_b32_e32 v57, v54
	v_pk_mul_f32 v[56:57], v[98:99], v[56:57] op_sel_hi:[0,1]
	v_pk_fma_f32 v[56:57], v[32:33], v[56:57], v[8:9]
	v_mov_b32_e32 v54, v93
	v_cvt_pk_fp8_f32 v91, v56, v57
	v_pk_mul_f32 v[54:55], v[98:99], v[54:55] op_sel_hi:[0,1]
	v_pk_fma_f32 v[54:55], v[30:31], v[54:55], v[10:11]
	v_mov_b32_e32 v56, 0
	v_cvt_pk_fp8_f32 v91, v54, v55 op_sel:[0,0,1]
	v_pk_mul_f32 v[54:55], v[94:95], v[98:99] op_sel_hi:[1,0]
	v_mov_b32_e32 v57, 0
	v_pk_fma_f32 v[54:55], v[36:37], v[54:55], v[12:13]
	v_pk_fma_f32 v[52:53], v[34:35], v[52:53], v[14:15]
	v_cvt_pk_fp8_f32 v56, v54, v55
	v_pk_mul_f32 v[54:55], v[96:97], v[98:99] op_sel_hi:[1,0]
	v_pk_fma_f32 v[50:51], v[38:39], v[50:51], v[18:19]
	v_pk_fma_f32 v[54:55], v[40:41], v[54:55], v[16:17]
	v_cvt_pk_fp8_f32 v56, v52, v53 op_sel:[0,0,1]
	v_cvt_pk_fp8_f32 v57, v54, v55
	s_waitcnt vmcnt(1)
	v_mov_b64_e32 v[52:53], v[70:71]
	v_mov_b64_e32 v[54:55], v[68:69]
	v_mov_b64_e32 v[68:69], v[78:79]
	v_cvt_pk_fp8_f32 v57, v50, v51 op_sel:[0,0,1]
	global_store_dword v[100:101], v90, off
	global_store_dword v[100:101], v91, off offset:256
	global_store_dword v[100:101], v56, off offset:512
	global_store_dword v[100:101], v57, off offset:768
	s_waitcnt vmcnt(4)
	v_mov_b64_e32 v[50:51], v[72:73]
	v_mov_b64_e32 v[56:57], v[66:67]
	v_mov_b64_e32 v[66:67], v[80:81]
	v_mov_b64_e32 v[70:71], v[76:77]
	v_mov_b64_e32 v[72:73], v[74:75]
	v_mov_b64_e32 v[74:75], v[64:65]
	v_mov_b64_e32 v[76:77], v[62:63]
	v_mov_b64_e32 v[78:79], v[60:61]
	v_mov_b64_e32 v[80:81], v[58:59]
	v_mov_b64_e32 v[58:59], v[42:43]
	v_mov_b64_e32 v[60:61], v[44:45]
	v_mov_b64_e32 v[62:63], v[46:47]
	v_mov_b64_e32 v[64:65], v[48:49]
	s_cbranch_vccnz .LBB0_166

.LBB0_171:
	v_lshlrev_b32_e32 v91, 16, v65
	v_lshlrev_b32_e32 v90, 16, v64
	v_and_b32_e32 v65, 0xffff0000, v65
	v_and_b32_e32 v64, 0xffff0000, v64
	v_pk_mul_f32 v[98:99], v[64:65], v[64:65]
	v_lshlrev_b32_e32 v93, 16, v63
	v_lshlrev_b32_e32 v92, 16, v62
	v_and_b32_e32 v63, 0xffff0000, v63
	v_and_b32_e32 v62, 0xffff0000, v62
	v_pk_fma_f32 v[98:99], v[90:91], v[90:91], v[98:99]
	v_lshlrev_b32_e32 v94, 16, v60
	v_and_b32_e32 v95, 0xffff0000, v60
	v_lshlrev_b32_e32 v60, 16, v61
	v_lshlrev_b32_e32 v96, 16, v58
	v_pk_add_f32 v[98:99], v[98:99], v[98:99] op_sel_hi:[0,1]
	v_pk_mul_f32 v[100:101], v[62:63], v[62:63]
	v_and_b32_e32 v61, 0xffff0000, v61
	v_pk_fma_f32 v[100:101], v[92:93], v[92:93], v[100:101]
	v_mul_f32_e32 v97, v94, v94
	v_mul_f32_e32 v103, v95, v95
	v_mul_f32_e32 v98, v60, v60
	v_mov_b32_e32 v102, v96
	v_and_b32_e32 v108, 0xffff0000, v58
	v_lshlrev_b32_e32 v58, 16, v59
	v_and_b32_e32 v59, 0xffff0000, v59
	v_pk_add_f32 v[100:101], v[100:101], v[100:101] op_sel_hi:[0,1]
	v_pk_fma_f32 v[104:105], v[60:61], v[60:61], v[98:99] op_sel_hi:[1,1,0]
	v_pk_add_f32 v[102:103], v[96:97], v[102:103]
	v_mul_f32_e32 v104, v108, v108
	v_mul_f32_e32 v100, v58, v58
	v_mul_f32_e32 v98, v59, v59
	v_mul_f32_e32 v106, v96, v96
	v_mov_b32_e32 v107, v103
	v_pk_add_f32 v[102:103], v[106:107], v[104:105]
	v_pk_add_f32 v[98:99], v[100:101], v[98:99]
	s_ashr_i32 s5, s4, 31
	v_pk_add_f32 v[98:99], v[102:103], v[98:99]
	v_mov_b32_e32 v102, v90
	v_add_f32_e32 v97, v98, v99
	s_nop 1
	v_add_f32_dpp v97, v97, v97 row_ror:8 row_mask:0xf bank_mask:0xf
	s_nop 1
	v_add_f32_dpp v97, v97, v97 row_ror:4 row_mask:0xf bank_mask:0xf
	s_nop 1
	v_add_f32_dpp v97, v97, v97 row_ror:2 row_mask:0xf bank_mask:0xf
	s_nop 1
	v_add_f32_dpp v97, v97, v97 row_ror:1 row_mask:0xf bank_mask:0xf
	s_nop 0
	v_readlane_b32 s14, v97, 0
	v_readlane_b32 s15, v97, 16
	v_readlane_b32 s16, v97, 32
	v_readlane_b32 s17, v97, 48
	v_mov_b32_e32 v97, s14
	v_add_f32_e32 v97, s15, v97
	v_add_f32_e32 v97, s16, v97
	v_add_f32_e32 v97, s17, v97
	v_mov_b32_e32 v103, v64
	v_mov_b32_e32 v90, 0
	v_mov_b32_e32 v64, v91
	v_mov_b32_e32 v91, 0
	s_lshl_b64 s[0:1], s[4:5], 10
	v_lshl_add_u64 v[100:101], v[24:25], 0, s[0:1]
	s_andn2_b64 vcc, exec, s[6:7]
	v_fmamk_f32 v97, v97, 0x3a800000, v210
	v_rsq_f32_e32 v98, v97
	v_mov_b32_e32 v97, v108
	v_pk_mul_f32 v[102:103], v[98:99], v[102:103] op_sel_hi:[0,1]
	v_pk_fma_f32 v[102:103], v[28:29], v[102:103], v[4:5]
	v_pk_mul_f32 v[64:65], v[98:99], v[64:65] op_sel_hi:[0,1]
	v_cvt_pk_fp8_f32 v90, v102, v103
	v_pk_fma_f32 v[64:65], v[26:27], v[64:65], v[6:7]
	v_pk_mul_f32 v[60:61], v[60:61], v[98:99] op_sel_hi:[1,0]
	v_pk_mul_f32 v[58:59], v[58:59], v[98:99] op_sel_hi:[1,0]
	v_cvt_pk_fp8_f32 v90, v64, v65 op_sel:[0,0,1]
	v_mov_b32_e32 v64, v92
	v_mov_b32_e32 v65, v62
	v_pk_mul_f32 v[64:65], v[98:99], v[64:65] op_sel_hi:[0,1]
	v_pk_fma_f32 v[64:65], v[32:33], v[64:65], v[8:9]
	v_mov_b32_e32 v62, v93
	v_cvt_pk_fp8_f32 v91, v64, v65
	v_pk_mul_f32 v[62:63], v[98:99], v[62:63] op_sel_hi:[0,1]
	v_pk_fma_f32 v[62:63], v[30:31], v[62:63], v[10:11]
	v_mov_b32_e32 v64, 0
	v_cvt_pk_fp8_f32 v91, v62, v63 op_sel:[0,0,1]
	v_pk_mul_f32 v[62:63], v[94:95], v[98:99] op_sel_hi:[1,0]
	v_mov_b32_e32 v65, 0
	v_pk_fma_f32 v[62:63], v[36:37], v[62:63], v[12:13]
	v_pk_fma_f32 v[60:61], v[34:35], v[60:61], v[14:15]
	v_cvt_pk_fp8_f32 v64, v62, v63
	v_pk_mul_f32 v[62:63], v[96:97], v[98:99] op_sel_hi:[1,0]
	v_pk_fma_f32 v[58:59], v[38:39], v[58:59], v[18:19]
	v_pk_fma_f32 v[62:63], v[40:41], v[62:63], v[16:17]
	v_cvt_pk_fp8_f32 v64, v60, v61 op_sel:[0,0,1]
	v_cvt_pk_fp8_f32 v65, v62, v63
	v_mov_b64_e32 v[62:63], v[76:77]
	v_mov_b64_e32 v[60:61], v[78:79]
	v_cvt_pk_fp8_f32 v65, v58, v59 op_sel:[0,0,1]
	v_cndmask_b32_e64 v58, 0, 1, s[6:7]
	global_store_dword v[100:101], v90, off
	global_store_dword v[100:101], v91, off offset:256
	global_store_dword v[100:101], v64, off offset:512
	global_store_dword v[100:101], v65, off offset:768
	v_cmp_ne_u32_e64 s[0:1], 1, v58
	v_mov_b64_e32 v[64:65], v[74:75]
	v_mov_b64_e32 v[58:59], v[80:81]
	s_cbranch_vccnz .LBB0_173
	s_add_i32 s6, s4, 5
	s_ashr_i32 s7, s6, 31
	s_lshl_b64 s[6:7], s[6:7], 11
	v_lshl_add_u64 v[64:65], v[22:23], 0, s[6:7]
	global_load_dwordx2 v[58:59], v[64:65], off
	global_load_dwordx2 v[60:61], v[64:65], off offset:512
	global_load_dwordx2 v[62:63], v[64:65], off offset:1024
	s_nop 0
	global_load_dwordx2 v[64:65], v[64:65], off offset:1536
.LBB0_173:
	v_lshlrev_b32_e32 v91, 16, v81
	v_lshlrev_b32_e32 v90, 16, v80
	v_and_b32_e32 v81, 0xffff0000, v81
	v_and_b32_e32 v80, 0xffff0000, v80
	v_pk_mul_f32 v[98:99], v[80:81], v[80:81]
	v_lshlrev_b32_e32 v93, 16, v79
	v_lshlrev_b32_e32 v92, 16, v78
	v_and_b32_e32 v79, 0xffff0000, v79
	v_and_b32_e32 v78, 0xffff0000, v78
	v_pk_fma_f32 v[98:99], v[90:91], v[90:91], v[98:99]
	v_lshlrev_b32_e32 v94, 16, v76
	v_and_b32_e32 v95, 0xffff0000, v76
	v_lshlrev_b32_e32 v76, 16, v77
	v_lshlrev_b32_e32 v96, 16, v74
	v_pk_add_f32 v[98:99], v[98:99], v[98:99] op_sel_hi:[0,1]
	v_pk_mul_f32 v[100:101], v[78:79], v[78:79]
	v_and_b32_e32 v77, 0xffff0000, v77
	v_pk_fma_f32 v[100:101], v[92:93], v[92:93], v[100:101]
	v_mul_f32_e32 v97, v94, v94
	v_mul_f32_e32 v103, v95, v95
	v_mul_f32_e32 v98, v76, v76
	v_mov_b32_e32 v102, v96
	v_and_b32_e32 v108, 0xffff0000, v74
	v_lshlrev_b32_e32 v74, 16, v75
	v_and_b32_e32 v75, 0xffff0000, v75
	v_pk_add_f32 v[100:101], v[100:101], v[100:101] op_sel_hi:[0,1]
	v_pk_fma_f32 v[104:105], v[76:77], v[76:77], v[98:99] op_sel_hi:[1,1,0]
	v_pk_add_f32 v[102:103], v[96:97], v[102:103]
	v_mul_f32_e32 v104, v108, v108
	v_mul_f32_e32 v100, v74, v74
	v_mul_f32_e32 v98, v75, v75
	v_mul_f32_e32 v106, v96, v96
	v_mov_b32_e32 v107, v103
	v_pk_add_f32 v[102:103], v[106:107], v[104:105]
	v_pk_add_f32 v[98:99], v[100:101], v[98:99]
	s_add_i32 s6, s4, 1
	v_pk_add_f32 v[98:99], v[102:103], v[98:99]
	v_mov_b32_e32 v102, v90
	v_add_f32_e32 v97, v98, v99
	s_nop 1
	v_add_f32_dpp v97, v97, v97 row_ror:8 row_mask:0xf bank_mask:0xf
	s_nop 1
	v_add_f32_dpp v97, v97, v97 row_ror:4 row_mask:0xf bank_mask:0xf
	s_nop 1
	v_add_f32_dpp v97, v97, v97 row_ror:2 row_mask:0xf bank_mask:0xf
	s_nop 1
	v_add_f32_dpp v97, v97, v97 row_ror:1 row_mask:0xf bank_mask:0xf
	s_nop 0
	v_readlane_b32 s14, v97, 0
	v_readlane_b32 s15, v97, 16
	v_readlane_b32 s16, v97, 32
	v_readlane_b32 s17, v97, 48
	v_mov_b32_e32 v97, s14
	v_add_f32_e32 v97, s15, v97
	v_add_f32_e32 v97, s16, v97
	v_add_f32_e32 v97, s17, v97
	v_mov_b32_e32 v103, v80
	v_mov_b32_e32 v90, 0
	v_mov_b32_e32 v80, v91
	v_mov_b32_e32 v91, 0
	s_ashr_i32 s7, s6, 31
	s_lshl_b64 s[6:7], s[6:7], 10
	v_lshl_add_u64 v[100:101], v[24:25], 0, s[6:7]
	s_and_b64 vcc, exec, s[0:1]
	v_fmamk_f32 v97, v97, 0x3a800000, v210
	v_rsq_f32_e32 v98, v97
	v_mov_b32_e32 v97, v108
	v_pk_mul_f32 v[102:103], v[98:99], v[102:103] op_sel_hi:[0,1]
	v_pk_fma_f32 v[102:103], v[28:29], v[102:103], v[4:5]
	v_pk_mul_f32 v[80:81], v[98:99], v[80:81] op_sel_hi:[0,1]
	v_cvt_pk_fp8_f32 v90, v102, v103
	v_pk_fma_f32 v[80:81], v[26:27], v[80:81], v[6:7]
	v_pk_mul_f32 v[76:77], v[76:77], v[98:99] op_sel_hi:[1,0]
	v_pk_mul_f32 v[74:75], v[74:75], v[98:99] op_sel_hi:[1,0]
	v_cvt_pk_fp8_f32 v90, v80, v81 op_sel:[0,0,1]
	v_mov_b32_e32 v80, v92
	v_mov_b32_e32 v81, v78
	v_pk_mul_f32 v[80:81], v[98:99], v[80:81] op_sel_hi:[0,1]
	v_pk_fma_f32 v[80:81], v[32:33], v[80:81], v[8:9]
	v_mov_b32_e32 v78, v93
	v_cvt_pk_fp8_f32 v91, v80, v81
	v_pk_mul_f32 v[78:79], v[98:99], v[78:79] op_sel_hi:[0,1]
	v_pk_fma_f32 v[78:79], v[30:31], v[78:79], v[10:11]
	v_mov_b32_e32 v80, 0
	v_cvt_pk_fp8_f32 v91, v78, v79 op_sel:[0,0,1]
	v_pk_mul_f32 v[78:79], v[94:95], v[98:99] op_sel_hi:[1,0]
	v_mov_b32_e32 v81, 0
	v_pk_fma_f32 v[78:79], v[36:37], v[78:79], v[12:13]
	v_pk_fma_f32 v[76:77], v[34:35], v[76:77], v[14:15]
	v_cvt_pk_fp8_f32 v80, v78, v79
	v_pk_mul_f32 v[78:79], v[96:97], v[98:99] op_sel_hi:[1,0]
	v_pk_fma_f32 v[74:75], v[38:39], v[74:75], v[18:19]
	v_pk_fma_f32 v[78:79], v[40:41], v[78:79], v[16:17]
	v_cvt_pk_fp8_f32 v80, v76, v77 op_sel:[0,0,1]
	v_cvt_pk_fp8_f32 v81, v78, v79
	v_mov_b64_e32 v[78:79], v[68:69]
	v_mov_b64_e32 v[76:77], v[70:71]
	v_cvt_pk_fp8_f32 v81, v74, v75 op_sel:[0,0,1]
	global_store_dword v[100:101], v90, off
	global_store_dword v[100:101], v91, off offset:256
	global_store_dword v[100:101], v80, off offset:512
	global_store_dword v[100:101], v81, off offset:768
	v_mov_b64_e32 v[80:81], v[66:67]
	v_mov_b64_e32 v[74:75], v[72:73]
	s_cbranch_vccnz .LBB0_175
	s_add_i32 s6, s4, 6
	s_ashr_i32 s7, s6, 31
	s_lshl_b64 s[6:7], s[6:7], 11
	v_lshl_add_u64 v[80:81], v[22:23], 0, s[6:7]
	global_load_dwordx2 v[74:75], v[80:81], off
	global_load_dwordx2 v[76:77], v[80:81], off offset:512
	global_load_dwordx2 v[78:79], v[80:81], off offset:1024
	s_nop 0
	global_load_dwordx2 v[80:81], v[80:81], off offset:1536
.LBB0_175:
	v_lshlrev_b32_e32 v91, 16, v73
	v_lshlrev_b32_e32 v90, 16, v72
	v_and_b32_e32 v73, 0xffff0000, v73
	v_and_b32_e32 v72, 0xffff0000, v72
	v_pk_mul_f32 v[98:99], v[72:73], v[72:73]
	v_lshlrev_b32_e32 v93, 16, v71
	v_lshlrev_b32_e32 v92, 16, v70
	v_and_b32_e32 v71, 0xffff0000, v71
	v_and_b32_e32 v70, 0xffff0000, v70
	v_pk_fma_f32 v[98:99], v[90:91], v[90:91], v[98:99]
	v_lshlrev_b32_e32 v94, 16, v68
	v_and_b32_e32 v95, 0xffff0000, v68
	v_lshlrev_b32_e32 v68, 16, v69
	v_lshlrev_b32_e32 v96, 16, v66
	v_pk_add_f32 v[98:99], v[98:99], v[98:99] op_sel_hi:[0,1]
	v_pk_mul_f32 v[100:101], v[70:71], v[70:71]
	v_and_b32_e32 v69, 0xffff0000, v69
	v_pk_fma_f32 v[100:101], v[92:93], v[92:93], v[100:101]
	v_mul_f32_e32 v97, v94, v94
	v_mul_f32_e32 v103, v95, v95
	v_mul_f32_e32 v98, v68, v68
	v_mov_b32_e32 v102, v96
	v_and_b32_e32 v108, 0xffff0000, v66
	v_lshlrev_b32_e32 v66, 16, v67
	v_and_b32_e32 v67, 0xffff0000, v67
	v_pk_add_f32 v[100:101], v[100:101], v[100:101] op_sel_hi:[0,1]
	v_pk_fma_f32 v[104:105], v[68:69], v[68:69], v[98:99] op_sel_hi:[1,1,0]
	v_pk_add_f32 v[102:103], v[96:97], v[102:103]
	v_mul_f32_e32 v104, v108, v108
	v_mul_f32_e32 v100, v66, v66
	v_mul_f32_e32 v98, v67, v67
	v_mul_f32_e32 v106, v96, v96
	v_mov_b32_e32 v107, v103
	v_pk_add_f32 v[102:103], v[106:107], v[104:105]
	v_pk_add_f32 v[98:99], v[100:101], v[98:99]
	s_add_i32 s6, s4, 2
	v_pk_add_f32 v[98:99], v[102:103], v[98:99]
	v_mov_b32_e32 v102, v90
	v_add_f32_e32 v97, v98, v99
	s_nop 1
	v_add_f32_dpp v97, v97, v97 row_ror:8 row_mask:0xf bank_mask:0xf
	s_nop 1
	v_add_f32_dpp v97, v97, v97 row_ror:4 row_mask:0xf bank_mask:0xf
	s_nop 1
	v_add_f32_dpp v97, v97, v97 row_ror:2 row_mask:0xf bank_mask:0xf
	s_nop 1
	v_add_f32_dpp v97, v97, v97 row_ror:1 row_mask:0xf bank_mask:0xf
	s_nop 0
	v_readlane_b32 s14, v97, 0
	v_readlane_b32 s15, v97, 16
	v_readlane_b32 s16, v97, 32
	v_readlane_b32 s17, v97, 48
	v_mov_b32_e32 v97, s14
	v_add_f32_e32 v97, s15, v97
	v_add_f32_e32 v97, s16, v97
	v_add_f32_e32 v97, s17, v97
	v_mov_b32_e32 v103, v72
	v_mov_b32_e32 v90, 0
	v_mov_b32_e32 v72, v91
	v_mov_b32_e32 v91, 0
	s_ashr_i32 s7, s6, 31
	s_lshl_b64 s[6:7], s[6:7], 10
	v_lshl_add_u64 v[100:101], v[24:25], 0, s[6:7]
	s_and_b64 vcc, exec, s[0:1]
	v_fmamk_f32 v97, v97, 0x3a800000, v210
	v_rsq_f32_e32 v98, v97
	v_mov_b32_e32 v97, v108
	v_pk_mul_f32 v[102:103], v[98:99], v[102:103] op_sel_hi:[0,1]
	v_pk_fma_f32 v[102:103], v[28:29], v[102:103], v[4:5]
	v_pk_mul_f32 v[72:73], v[98:99], v[72:73] op_sel_hi:[0,1]
	v_cvt_pk_fp8_f32 v90, v102, v103
	v_pk_fma_f32 v[72:73], v[26:27], v[72:73], v[6:7]
	v_pk_mul_f32 v[68:69], v[68:69], v[98:99] op_sel_hi:[1,0]
	v_pk_mul_f32 v[66:67], v[66:67], v[98:99] op_sel_hi:[1,0]
	v_cvt_pk_fp8_f32 v90, v72, v73 op_sel:[0,0,1]
	v_mov_b32_e32 v72, v92
	v_mov_b32_e32 v73, v70
	v_pk_mul_f32 v[72:73], v[98:99], v[72:73] op_sel_hi:[0,1]
	v_pk_fma_f32 v[72:73], v[32:33], v[72:73], v[8:9]
	v_mov_b32_e32 v70, v93
	v_cvt_pk_fp8_f32 v91, v72, v73
	v_pk_mul_f32 v[70:71], v[98:99], v[70:71] op_sel_hi:[0,1]
	v_pk_fma_f32 v[70:71], v[30:31], v[70:71], v[10:11]
	v_mov_b32_e32 v72, 0
	v_cvt_pk_fp8_f32 v91, v70, v71 op_sel:[0,0,1]
	v_pk_mul_f32 v[70:71], v[94:95], v[98:99] op_sel_hi:[1,0]
	v_mov_b32_e32 v73, 0
	v_pk_fma_f32 v[70:71], v[36:37], v[70:71], v[12:13]
	v_pk_fma_f32 v[68:69], v[34:35], v[68:69], v[14:15]
	v_cvt_pk_fp8_f32 v72, v70, v71
	v_pk_mul_f32 v[70:71], v[96:97], v[98:99] op_sel_hi:[1,0]
	v_pk_fma_f32 v[66:67], v[38:39], v[66:67], v[18:19]
	v_pk_fma_f32 v[70:71], v[40:41], v[70:71], v[16:17]
	v_cvt_pk_fp8_f32 v72, v68, v69 op_sel:[0,0,1]
	v_cvt_pk_fp8_f32 v73, v70, v71
	v_mov_b64_e32 v[70:71], v[52:53]
	v_mov_b64_e32 v[68:69], v[54:55]
	v_cvt_pk_fp8_f32 v73, v66, v67 op_sel:[0,0,1]
	global_store_dword v[100:101], v90, off
	global_store_dword v[100:101], v91, off offset:256
	global_store_dword v[100:101], v72, off offset:512
	global_store_dword v[100:101], v73, off offset:768
	v_mov_b64_e32 v[72:73], v[50:51]
	v_mov_b64_e32 v[66:67], v[56:57]
	s_cbranch_vccnz .LBB0_168
	s_add_i32 s0, s4, 7
	s_ashr_i32 s1, s0, 31
	s_lshl_b64 s[0:1], s[0:1], 11
	v_lshl_add_u64 v[72:73], v[22:23], 0, s[0:1]
	global_load_dwordx2 v[66:67], v[72:73], off
	global_load_dwordx2 v[68:69], v[72:73], off offset:512
	global_load_dwordx2 v[70:71], v[72:73], off offset:1024
	s_nop 0
	global_load_dwordx2 v[72:73], v[72:73], off offset:1536
	s_branch .LBB0_168
